# zero-state offload + chain index = 8x8 transpose of workgroup index (the two row-half chains of a (b,h,dir) share one XCD L2 for their KdT panels)
# speedup vs baseline: 1.0061x; 1.0061x over previous
.LBB0_694:
	s_and_b32 s3, s2, 7
	s_lshl_b32 s3, s3, 3
	s_lshr_b32 s4, s2, 3
	s_or_b32 s2, s3, s4
	s_lshl_b32 s3, s2, 1
	s_and_b32 s3, s3, 4
	s_bfe_u32 s4, s2, 0x20002
	s_or_b32 s3, s3, s4
	s_lshl_b32 s3, s3, 2
	v_mov_b32_e32 v2, s3
	global_load_dword v16, v2, s[66:67]
	v_mov_b32_e32 v17, v0
	s_mov_b32 s3, 64
	s_cmpk_gt_u32 s2, 0x1bf
	v_readfirstlane_b32 s8, v17
	s_cbranch_scc1 .LBB0_734
	v_ashrrev_i32_e32 v3, 31, v17
	v_lshrrev_b32_e32 v3, 26, v3
	v_add_u32_e32 v3, v17, v3
	v_ashrrev_i32_e32 v10, 6, v3
	v_bfe_i32 v3, v17, 27, 1
	v_lshlrev_b32_e32 v2, 4, v17
	v_lshrrev_b32_e32 v3, 22, v3
	v_add_u32_e32 v3, v2, v3
	v_and_b32_e32 v3, 0xfffffc00, v3
	v_sub_u32_e32 v3, v2, v3
	v_lshrrev_b32_e32 v4, 4, v3
	v_bitop3_b32 v4, v4, v3, 32 bitop3:0x6c
	v_ashrrev_i32_e32 v3, 31, v3
	v_lshrrev_b32_e32 v3, 26, v3
	v_add_u32_e32 v3, v4, v3
	v_ashrrev_i32_e32 v11, 6, v3
	v_lshlrev_b32_e32 v5, 3, v10
	v_mul_i32_i24_e32 v6, 64, v11
	v_and_b32_e32 v5, -16, v5
	v_sub_u32_e32 v4, v4, v6
	v_add_u32_e32 v3, v11, v5
	v_lshlrev_b32_e32 v5, 5, v10
	v_ashrrev_i16_sdwa v4, v236, sext(v4) dst_sel:DWORD dst_unused:UNUSED_PAD src0_sel:DWORD src1_sel:BYTE_0
	v_and_b32_e32 v5, 32, v5
	v_bfe_i32 v12, v4, 0, 16
	v_add_u32_e32 v4, v5, v12
	v_lshlrev_b32_e32 v5, 1, v3
	v_lshrrev_b32_e32 v6, 2, v3
	v_and_b32_e32 v5, 24, v5
	v_and_b32_e32 v6, 4, v6
	v_and_b32_e32 v7, 3, v11
	s_mov_b32 s6, 0x3fffe0
	v_or3_b32 v6, v7, v6, v5
	v_and_or_b32 v5, v3, s6, v5
	v_lshlrev_b32_e32 v3, 11, v3
	v_lshl_add_u32 v198, v4, 1, v3
	v_lshlrev_b32_e32 v3, 2, v5
	v_and_b32_e32 v3, 0xffffc0, v3
	v_lshrrev_b32_e32 v4, 3, v4
	v_add_u32_e32 v3, v3, v4
	v_lshlrev_b32_e32 v4, 4, v6
	v_and_b32_e32 v4, 0xf0, v4
	v_add_u32_e32 v2, 0x2000, v2
	v_lshl_or_b32 v200, v3, 8, v4
	v_ashrrev_i32_e32 v3, 31, v2
	v_lshrrev_b32_e32 v3, 22, v3
	v_add_u32_e32 v3, v2, v3
	v_ashrrev_i32_e32 v13, 10, v3
	v_mul_i32_i24_e32 v3, 0x400, v13
	v_sub_u32_e32 v2, v2, v3
	v_lshrrev_b32_e32 v3, 4, v2
	v_bitop3_b32 v2, v3, v2, 32 bitop3:0x6c
	v_ashrrev_i32_e32 v4, 31, v2
	v_lshrrev_b32_e32 v4, 26, v4
	s_add_u32 s34, s74, 0x16a00000
	v_add_u32_e32 v4, v2, v4
	s_addc_u32 s35, s75, 0
	v_ashrrev_i32_e32 v14, 6, v4
	v_and_b32_e32 v4, 0xc0, v4
	s_add_u32 s4, s74, 0x1ea00000
	v_lshlrev_b32_e32 v3, 3, v13
	v_sub_u32_e32 v2, v2, v4
	s_addc_u32 s5, s75, 0
	v_and_b32_e32 v3, -16, v3
	v_lshlrev_b32_e32 v5, 5, v13
	v_ashrrev_i16_sdwa v2, v236, sext(v2) dst_sel:DWORD dst_unused:UNUSED_PAD src0_sel:DWORD src1_sel:BYTE_0
	s_lshr_b32 s74, s2, 6
	s_ashr_i32 s9, s8, 8
	s_ashr_i32 s10, s8, 6
	v_add_u32_e32 v3, v14, v3
	v_and_b32_e32 v5, 32, v5
	v_bfe_i32 v15, v2, 0, 16
	s_bfe_u32 s49, s2, 0x10001
	s_sub_i32 s11, 7, s74
	v_add_u32_e32 v2, v5, v15
	v_lshlrev_b32_e32 v4, 1, v3
	v_lshrrev_b32_e32 v5, 2, v3
	s_cmp_eq_u32 s49, 0
	v_and_b32_e32 v4, 24, v4
	v_and_b32_e32 v5, 4, v5
	v_and_b32_e32 v6, 3, v14
	s_cselect_b64 s[36:37], -1, 0
	v_or3_b32 v5, v6, v5, v4
	v_and_or_b32 v4, v3, s6, v4
	s_and_b64 s[6:7], s[36:37], exec
	s_cselect_b32 s6, s74, s11
	s_lshl_b32 s7, s2, 1
	s_and_b32 s12, s7, 0x78
	s_or_b32 s72, s6, s12
	s_lshl_b32 s6, s2, 8
	s_and_b32 s11, s6, 0x100
	s_lshl_b32 s13, s11, 11
	s_lshl_b64 s[6:7], s[72:73], 20
	s_add_u32 s6, s34, s6
	s_addc_u32 s7, s35, s7
	s_add_u32 s38, s6, s13
	s_addc_u32 s39, s7, 0
	s_lshl_b64 s[6:7], s[72:73], 19
	s_add_u32 s13, s4, s6
	v_lshlrev_b32_e32 v3, 11, v3
	s_addc_u32 s7, s5, s7
	s_lshl_b32 s6, s10, 10
	s_lshl_b32 s14, s49, 18
	v_lshl_add_u32 v202, v2, 1, v3
	v_lshlrev_b32_e32 v3, 2, v4
	s_add_u32 s54, s13, s14
	v_and_b32_e32 v3, 0xffffc0, v3
	v_lshrrev_b32_e32 v2, 3, v2
	s_addc_u32 s55, s7, 0
	s_add_i32 s7, s6, 0
	v_add_u32_e32 v2, v3, v2
	v_lshlrev_b32_e32 v3, 4, v5
	s_add_i32 s68, s7, 0x10000
	s_add_i32 s69, s7, 0x12000
	v_and_b32_e32 v3, 0xf0, v3
	s_mov_b32 m0, s68
	s_add_u32 s14, s54, 0x20000
	v_lshl_or_b32 v208, v2, 8, v3
	global_load_lds_dwordx4 v200, s[54:55]
	s_mov_b32 m0, s69
	s_addc_u32 s15, s55, 0
	s_add_i32 s70, s7, 0x14000
	global_load_lds_dwordx4 v208, s[54:55]
	s_mov_b32 m0, s70
	s_add_i32 s71, s7, 0x16000
	global_load_lds_dwordx4 v200, s[14:15]
	s_mov_b32 m0, s71
	s_add_i32 s84, s7, 0x2000
	global_load_lds_dwordx4 v208, s[14:15]
	s_mov_b32 m0, s7
	s_add_u32 s14, s38, 0x40000
	global_load_lds_dwordx4 v198, s[38:39]
	s_mov_b32 m0, s84
	s_addc_u32 s15, s39, 0
	s_add_i32 s85, s7, 0x4000
	global_load_lds_dwordx4 v202, s[38:39]
	s_mov_b32 m0, s85
	s_add_i32 s86, s7, 0x6000
	global_load_lds_dwordx4 v198, s[14:15]
	s_mov_b32 m0, s86
	v_mov_b32_e32 v201, v67
	global_load_lds_dwordx4 v202, s[14:15]
	v_mov_b32_e32 v209, v67
	v_mov_b32_e32 v199, v67
	v_mov_b32_e32 v203, v67
	s_cmp_eq_u32 s9, 1
	v_lshl_add_u64 v[8:9], s[54:55], 0, v[200:201]
	v_lshl_add_u64 v[6:7], s[54:55], 0, v[208:209]
	v_lshl_add_u64 v[2:3], s[38:39], 0, v[198:199]
	s_cselect_b64 s[40:41], -1, 0
	s_cmp_lg_u32 s9, 1
	v_lshl_add_u64 v[4:5], s[38:39], 0, v[202:203]
	s_cbranch_scc1 .LBB0_697
	s_barrier

.LBB0_746:
	s_waitcnt vmcnt(0)
	v_readlane_b32 s88, v254, 61
	v_readlane_b32 s50, v255, 0
	s_barrier
	v_readlane_b32 s87, v254, 60
	v_readlane_b32 s89, v254, 62
	v_readlane_b32 s51, v255, 1
	s_sub_i32 s4, s2, 64
	s_and_b32 s5, s4, 7
	s_lshl_b32 s5, s5, 3
	s_lshr_b32 s4, s4, 3
	s_or_b32 s4, s5, s4
	s_lshr_b32 s5, s4, 2
	s_bfe_u32 s6, s4, 0x10001
	s_and_b32 s7, s4, 1
	s_lshl_b32 s5, s5, 3
	s_mul_i32 s10, s6, 7
	s_add_i32 s5, s5, s10
	s_lshl_b32 s5, s5, 20
	s_lshl_b32 s7, s7, 19
	s_add_i32 s5, s5, s7
	s_lshl_b32 s6, s6, 9
	s_add_i32 s5, s5, s6
	s_addk_i32 s5, 0x400
	s_load_dwordx2 s[8:9], s[88:89], 0x88
	v_lshrrev_b32_e32 v2, 5, v0
	v_lshlrev_b32_e32 v2, 11, v2
	v_and_b32_e32 v3, 31, v0
	v_lshl_or_b32 v2, v3, 4, v2
	v_mov_b32_e32 v3, 0
	v_mov_b32_e32 v4, 0
	v_mov_b32_e32 v5, 0
	v_mov_b32_e32 v6, 0
	v_mov_b32_e32 v7, 0
	s_waitcnt lgkmcnt(0)
	s_add_u32 s8, s8, 0x16a00000
	s_addc_u32 s9, s9, 0
	s_add_u32 s8, s8, s5
	s_addc_u32 s9, s9, 0
	v_lshl_add_u64 v[2:3], v[2:3], 0, s[8:9]
	s_mov_b32 s10, 0x8000
	s_mov_b32 s11, 0
	global_store_dwordx4 v[2:3], v[4:7], off
	v_lshl_add_u64 v[2:3], v[2:3], 0, s[10:11]
	global_store_dwordx4 v[2:3], v[4:7], off
	v_lshl_add_u64 v[2:3], v[2:3], 0, s[10:11]
	global_store_dwordx4 v[2:3], v[4:7], off
	v_lshl_add_u64 v[2:3], v[2:3], 0, s[10:11]
	global_store_dwordx4 v[2:3], v[4:7], off
	v_lshl_add_u64 v[2:3], v[2:3], 0, s[10:11]
	global_store_dwordx4 v[2:3], v[4:7], off
	v_lshl_add_u64 v[2:3], v[2:3], 0, s[10:11]
	global_store_dwordx4 v[2:3], v[4:7], off
	v_lshl_add_u64 v[2:3], v[2:3], 0, s[10:11]
	global_store_dwordx4 v[2:3], v[4:7], off
	v_lshl_add_u64 v[2:3], v[2:3], 0, s[10:11]
	global_store_dwordx4 v[2:3], v[4:7], off
	v_lshl_add_u64 v[2:3], v[2:3], 0, s[10:11]
	global_store_dwordx4 v[2:3], v[4:7], off
	v_lshl_add_u64 v[2:3], v[2:3], 0, s[10:11]
	global_store_dwordx4 v[2:3], v[4:7], off
	v_lshl_add_u64 v[2:3], v[2:3], 0, s[10:11]
	global_store_dwordx4 v[2:3], v[4:7], off
	v_lshl_add_u64 v[2:3], v[2:3], 0, s[10:11]
	global_store_dwordx4 v[2:3], v[4:7], off
	v_lshl_add_u64 v[2:3], v[2:3], 0, s[10:11]
	global_store_dwordx4 v[2:3], v[4:7], off
	v_lshl_add_u64 v[2:3], v[2:3], 0, s[10:11]
	global_store_dwordx4 v[2:3], v[4:7], off
	v_lshl_add_u64 v[2:3], v[2:3], 0, s[10:11]
	global_store_dwordx4 v[2:3], v[4:7], off
	v_lshl_add_u64 v[2:3], v[2:3], 0, s[10:11]
	global_store_dwordx4 v[2:3], v[4:7], off
	s_cbranch_execz .LBB0_694
	s_branch .LBB0_734
